# final RMSNorm row loop: gamma row and output base hoisted out of the loop, no per-store drain; plus one priority raise per MFMA segment
# speedup vs baseline: 1.0095x; 1.0095x over previous
; __device__ __forceinline__ float f16_lo(unsigned u) { return (float)__builtin_bit_cast(h16x2, u)[0]; }
; __device__ __forceinline__ float f16_hi(unsigned u) { return (float)__builtin_bit_cast(h16x2, u)[1]; }
; #define GAS __attribute__((address_space(1)))
; __global__ void __launch_bounds__(NWAVES * 64, 2) mk_fwd(Args args) {
;     ...
;         { int m = gw; asm volatile("" : "+s"(m)); const GAS f32x4* gr = (const GAS f32x4*)ap->in[22] + ln;
;           for (; m < M; m += 2 * NGW) { f32x4 v[2][4]; float ss[2] = {0.f, 0.f};
; #pragma unroll
;               for (int r = 0; r < 2; ++r) { const GAS v2u* xr = (const GAS v2u*)(hx + (size_t)(m + r * NGW) * D) + ln;
; #pragma unroll
;                   for (int q = 0; q < 4; ++q) { const v2u hv = xr[64 * q]; v[r][q] = (f32x4){pg8::f16_lo(hv.x), pg8::f16_hi(hv.x), pg8::f16_lo(hv.y), pg8::f16_hi(hv.y)}; } }
; #pragma unroll
;               for (int r = 0; r < 2; ++r) {
; #pragma unroll
;                   for (int q = 0; q < 4; ++q) ss[r] += (v[r][q].x * v[r][q].x + v[r][q].y * v[r][q].y) + (v[r][q].z * v[r][q].z + v[r][q].w * v[r][q].w);
.LBB0_1355:
	s_cmpk_lt_i32 s72, 0x42
	s_cselect_b64 s[0:1], -1, 0
	s_cmpk_gt_i32 s73, 0x41
	s_cselect_b64 s[2:3], -1, 0
	s_and_b64 s[0:1], s[0:1], s[2:3]
	s_and_b64 vcc, exec, s[0:1]
	s_cbranch_vccz .LBB0_1359
	v_mov_b32_e32 v0, 0
	v_readlane_b32 s0, v254, 2
	s_cmpk_gt_i32 s60, 0x3fff
	s_cbranch_scc1 .LBB0_1359
	v_mov_b64_e32 v[2:3], s[66:67]
	global_load_dwordx2 v[8:9], v[2:3], off offset:176
	v_mbcnt_lo_u32_b32 v3, -1, v0
	v_mbcnt_hi_u32_b32 v16, -1, v3
	s_add_u32 s1, s80, 0x600000
	v_ashrrev_i32_e32 v17, 31, v16
	v_lshlrev_b32_e32 v4, 2, v16
	s_waitcnt lgkmcnt(0)
	v_mov_b64_e32 v[0:1], s[66:67]
	s_mov_b32 s0, 0x3a800000
	v_mov_b32_e32 v2, 0x358637bd
	s_addc_u32 s4, s81, 0
	s_lshl_b32 s5, s59, 4
	v_xor_b32_e32 v3, 4, v4
	v_xor_b32_e32 v10, 8, v4
	v_xor_b32_e32 v11, 16, v4
	v_xor_b32_e32 v12, 32, v4
	v_xor_b32_e32 v13, 64, v4
	v_xor_b32_e32 v14, 0x80, v4
	v_lshlrev_b64 v[4:5], 3, v[16:17]
	v_lshlrev_b64 v[6:7], 4, v[16:17]
	s_mov_b32 s6, 0x800000
	s_waitcnt vmcnt(0)
	v_lshl_add_u64 v[8:9], v[16:17], 4, v[8:9]
	global_load_dwordx4 v[72:75], v[8:9], off
	global_load_dwordx4 v[76:79], v[8:9], off offset:1024
	global_load_dwordx4 v[80:83], v[8:9], off offset:2048
	global_load_dwordx4 v[84:87], v[8:9], off offset:3072
	global_load_dwordx2 v[88:89], v[0:1], off offset:184
	s_waitcnt vmcnt(0)
	v_lshl_add_u64 v[88:89], v[88:89], 0, v[6:7]
.LBB0_1358:
	s_ashr_i32 s61, s60, 31
	s_lshl_b64 s[2:3], s[60:61], 11
	s_add_u32 s2, s1, s2
	s_addc_u32 s3, s4, s3
	v_lshl_add_u64 v[16:17], s[2:3], 0, v[4:5]
	global_load_dwordx2 v[20:21], v[16:17], off
	global_load_dwordx2 v[22:23], v[16:17], off offset:512
	global_load_dwordx2 v[24:25], v[16:17], off offset:1024
	s_add_i32 s2, s54, s60
	global_load_dwordx2 v[26:27], v[16:17], off offset:1536
	s_ashr_i32 s3, s2, 31
	s_lshl_b64 s[8:9], s[2:3], 11
	s_add_u32 s8, s1, s8
	s_addc_u32 s9, s4, s9
	v_lshl_add_u64 v[28:29], s[8:9], 0, v[4:5]
	global_load_dwordx2 v[30:31], v[28:29], off
	global_load_dwordx2 v[32:33], v[28:29], off offset:512
	global_load_dwordx2 v[34:35], v[28:29], off offset:1024
	global_load_dwordx2 v[36:37], v[28:29], off offset:1536
	s_lshl_b64 s[8:9], s[60:61], 12
	s_lshl_b64 s[2:3], s[2:3], 12
	s_add_i32 s60, s60, s5
	s_cmpk_lt_i32 s60, 0x4000
	s_waitcnt vmcnt(0)
	v_cvt_f32_f16_e32 v28, v20
	v_cvt_f32_f16_sdwa v29, v20 dst_sel:DWORD dst_unused:UNUSED_PAD src0_sel:WORD_1
	v_cvt_f32_f16_e32 v20, v21
	v_cvt_f32_f16_sdwa v21, v21 dst_sel:DWORD dst_unused:UNUSED_PAD src0_sel:WORD_1
	v_cvt_f32_f16_e32 v40, v22
	v_cvt_f32_f16_sdwa v41, v22 dst_sel:DWORD dst_unused:UNUSED_PAD src0_sel:WORD_1
	v_cvt_f32_f16_e32 v22, v23
	v_cvt_f32_f16_sdwa v23, v23 dst_sel:DWORD dst_unused:UNUSED_PAD src0_sel:WORD_1
	v_cvt_f32_f16_e32 v42, v24
	v_cvt_f32_f16_sdwa v43, v24 dst_sel:DWORD dst_unused:UNUSED_PAD src0_sel:WORD_1
	v_cvt_f32_f16_e32 v24, v25
	v_cvt_f32_f16_sdwa v25, v25 dst_sel:DWORD dst_unused:UNUSED_PAD src0_sel:WORD_1
	v_cvt_f32_f16_e32 v44, v26
	v_cvt_f32_f16_sdwa v45, v26 dst_sel:DWORD dst_unused:UNUSED_PAD src0_sel:WORD_1
	v_cvt_f32_f16_e32 v26, v27
	v_cvt_f32_f16_sdwa v27, v27 dst_sel:DWORD dst_unused:UNUSED_PAD src0_sel:WORD_1
	v_cvt_f32_f16_e32 v46, v30
	v_cvt_f32_f16_sdwa v47, v30 dst_sel:DWORD dst_unused:UNUSED_PAD src0_sel:WORD_1
	v_cvt_f32_f16_e32 v30, v31
	v_cvt_f32_f16_sdwa v31, v31 dst_sel:DWORD dst_unused:UNUSED_PAD src0_sel:WORD_1
	v_cvt_f32_f16_e32 v48, v32
	v_cvt_f32_f16_sdwa v49, v32 dst_sel:DWORD dst_unused:UNUSED_PAD src0_sel:WORD_1
	v_cvt_f32_f16_e32 v32, v33
	v_cvt_f32_f16_sdwa v33, v33 dst_sel:DWORD dst_unused:UNUSED_PAD src0_sel:WORD_1
	v_mov_b32_e32 v56, v29
	v_mov_b32_e32 v57, v21
	v_mov_b32_e32 v60, v41
	v_mov_b32_e32 v61, v23
	v_mov_b32_e32 v54, v28
	v_mov_b32_e32 v55, v20
	v_mov_b32_e32 v58, v40
	v_mov_b32_e32 v59, v22
	v_mul_f32_e32 v62, v43, v43
	v_mul_f32_e32 v64, v25, v25
	v_pk_mul_f32 v[56:57], v[56:57], v[56:57]
	v_pk_mul_f32 v[60:61], v[60:61], v[60:61]
	v_cvt_f32_f16_e32 v50, v34
	v_cvt_f32_f16_sdwa v51, v34 dst_sel:DWORD dst_unused:UNUSED_PAD src0_sel:WORD_1
	v_cvt_f32_f16_e32 v34, v35
	v_cvt_f32_f16_sdwa v35, v35 dst_sel:DWORD dst_unused:UNUSED_PAD src0_sel:WORD_1
	v_pk_mul_f32 v[68:69], v[26:27], v[26:27]
	v_pk_fma_f32 v[62:63], v[42:43], v[42:43], v[62:63] op_sel_hi:[1,1,0]
	v_pk_fma_f32 v[64:65], v[24:25], v[24:25], v[64:65] op_sel_hi:[1,1,0]
	v_pk_fma_f32 v[54:55], v[54:55], v[54:55], v[56:57]
	v_pk_fma_f32 v[56:57], v[58:59], v[58:59], v[60:61]
	v_cvt_f32_f16_e32 v52, v36
	v_cvt_f32_f16_sdwa v53, v36 dst_sel:DWORD dst_unused:UNUSED_PAD src0_sel:WORD_1
	v_cvt_f32_f16_e32 v36, v37
	v_cvt_f32_f16_sdwa v37, v37 dst_sel:DWORD dst_unused:UNUSED_PAD src0_sel:WORD_1
	v_pk_mul_f32 v[66:67], v[44:45], v[44:45]
	v_mov_b32_e32 v63, v68
	v_mov_b32_e32 v65, v69
	v_pk_add_f32 v[54:55], v[54:55], v[54:55] op_sel:[0,1] op_sel_hi:[1,0]
	v_pk_add_f32 v[56:57], v[56:57], v[56:57] op_sel:[0,1] op_sel_hi:[1,0]
	v_pk_add_f32 v[58:59], v[62:63], v[64:65]
	v_mov_b32_e32 v55, v66
	v_mov_b32_e32 v57, v67
	v_mov_b32_e32 v62, v47
	v_mov_b32_e32 v63, v31
	v_mov_b32_e32 v66, v49
	v_mov_b32_e32 v67, v33
	v_mov_b32_e32 v60, v46
	v_mov_b32_e32 v61, v30
	v_mov_b32_e32 v64, v48
	v_mov_b32_e32 v65, v32
	v_pk_add_f32 v[54:55], v[54:55], v[56:57]
	v_pk_mul_f32 v[56:57], v[62:63], v[62:63]
	v_pk_mul_f32 v[62:63], v[66:67], v[66:67]
	v_mul_f32_e32 v68, v51, v51
	v_mul_f32_e32 v70, v35, v35
	v_pk_add_f32 v[54:55], v[54:55], v[58:59]
	v_pk_fma_f32 v[56:57], v[60:61], v[60:61], v[56:57]
	v_pk_fma_f32 v[58:59], v[64:65], v[64:65], v[62:63]
	v_pk_fma_f32 v[66:67], v[50:51], v[50:51], v[68:69] op_sel_hi:[1,1,0]
	v_pk_add_f32 v[56:57], v[56:57], v[56:57] op_sel:[0,1] op_sel_hi:[1,0]
	v_pk_add_f32 v[58:59], v[58:59], v[58:59] op_sel:[0,1] op_sel_hi:[1,0]
	v_pk_fma_f32 v[60:61], v[34:35], v[34:35], v[70:71] op_sel_hi:[1,1,0]
	v_pk_mul_f32 v[62:63], v[52:53], v[52:53]
	v_pk_mul_f32 v[64:65], v[36:37], v[36:37]
	v_mov_b32_e32 v57, v62
	v_mov_b32_e32 v59, v63
	v_mov_b32_e32 v67, v64
	v_mov_b32_e32 v61, v65
	v_pk_add_f32 v[56:57], v[56:57], v[58:59]
	v_pk_add_f32 v[58:59], v[66:67], v[60:61]
	s_waitcnt lgkmcnt(0)
; #define GAS __attribute__((address_space(1)))
; __device__ __forceinline__ float wave_sum(float v, int lane) {
; #pragma unroll
;     for (int o = 1; o < 64; o <<= 1) v += __builtin_bit_cast(float, __builtin_amdgcn_ds_bpermute((lane ^ o) << 2, __builtin_bit_cast(int, v)));
;     return v;
; __global__ void __launch_bounds__(NWAVES * 64, 2) mk_fwd(Args args) {
;     ...
;               for (int r = 0; r < 2; ++r) {
; #pragma unroll
;                   for (int q = 0; q < 4; ++q) ss[r] += (v[r][q].x * v[r][q].x + v[r][q].y * v[r][q].y) + (v[r][q].z * v[r][q].z + v[r][q].w * v[r][q].w);
;                   const float rstd = rsqrtf(wave_sum(ss[r], ln) * (1.f / D) + EPS); GAS f32x4* o = (GAS f32x4*)(ap->out + (size_t)(m + r * NGW) * D) + ln;
; #pragma unroll
;                   for (int q = 0; q < 4; ++q) o[64 * q] = v[r][q] * rstd * gr[64 * q]; } } }
	v_lshl_add_u64 v[38:39], v[88:89], 0, s[8:9]
	v_pk_add_f32 v[56:57], v[56:57], v[58:59]
	v_mov_b32_e32 v59, v54
	v_mov_b32_e32 v58, v56
	v_mov_b32_e32 v54, v57
	v_pk_add_f32 v[54:55], v[58:59], v[54:55]
	ds_bpermute_b32 v57, v3, v55
	ds_bpermute_b32 v56, v3, v54
	s_waitcnt lgkmcnt(0)
	v_pk_add_f32 v[54:55], v[54:55], v[56:57]
	ds_bpermute_b32 v57, v10, v55
	ds_bpermute_b32 v56, v10, v54
	s_waitcnt lgkmcnt(0)
	v_pk_add_f32 v[54:55], v[54:55], v[56:57]
	ds_bpermute_b32 v57, v11, v55
	ds_bpermute_b32 v56, v11, v54
	s_waitcnt lgkmcnt(0)
	v_pk_add_f32 v[54:55], v[54:55], v[56:57]
	ds_bpermute_b32 v57, v12, v55
	ds_bpermute_b32 v56, v12, v54
	s_waitcnt lgkmcnt(0)
	v_pk_add_f32 v[54:55], v[54:55], v[56:57]
	ds_bpermute_b32 v57, v13, v55
	ds_bpermute_b32 v56, v13, v54
	s_waitcnt lgkmcnt(0)
	v_pk_add_f32 v[54:55], v[54:55], v[56:57]
	ds_bpermute_b32 v57, v14, v55
	ds_bpermute_b32 v56, v14, v54
	s_waitcnt lgkmcnt(0)
	v_pk_add_f32 v[54:55], v[54:55], v[56:57]
	s_nop 0
	v_pk_fma_f32 v[54:55], v[54:55], s[0:1], v[2:3] op_sel_hi:[1,0,0]
	s_nop 0
	v_mul_f32_e32 v15, 0x4b800000, v55
	v_cmp_gt_f32_e32 vcc, s6, v55
	s_nop 1
	v_cndmask_b32_e32 v15, v55, v15, vcc
	v_rsq_f32_e32 v15, v15
	s_nop 0
	v_mul_f32_e32 v55, 0x45800000, v15
	v_cndmask_b32_e32 v56, v15, v55, vcc
	v_pk_mul_f32 v[28:29], v[56:57], v[28:29] op_sel_hi:[0,1]
	v_pk_mul_f32 v[20:21], v[56:57], v[20:21] op_sel_hi:[0,1]
	v_pk_mul_f32 v[18:19], v[20:21], v[74:75]
	v_pk_mul_f32 v[16:17], v[28:29], v[72:73]
	global_store_dwordx4 v[38:39], v[16:19], off sc1
	v_pk_mul_f32 v[20:21], v[56:57], v[22:23] op_sel_hi:[0,1]
	v_pk_mul_f32 v[22:23], v[56:57], v[40:41] op_sel_hi:[0,1]
	v_mul_f32_e32 v15, 0x4b800000, v54
	v_cmp_gt_f32_e32 vcc, s6, v54
	v_pk_mul_f32 v[90:91], v[22:23], v[76:77]
	v_pk_mul_f32 v[92:93], v[20:21], v[78:79]
	global_store_dwordx4 v[38:39], v[90:93], off offset:1024 sc1
	v_pk_mul_f32 v[20:21], v[56:57], v[24:25] op_sel_hi:[0,1]
	v_pk_mul_f32 v[22:23], v[56:57], v[42:43] op_sel_hi:[0,1]
	v_cndmask_b32_e32 v15, v54, v15, vcc
	v_rsq_f32_e32 v15, v15
	v_pk_mul_f32 v[94:95], v[22:23], v[80:81]
	v_pk_mul_f32 v[96:97], v[20:21], v[82:83]
	global_store_dwordx4 v[38:39], v[94:97], off offset:2048 sc1
	v_pk_mul_f32 v[20:21], v[56:57], v[26:27] op_sel_hi:[0,1]
	v_pk_mul_f32 v[22:23], v[56:57], v[44:45] op_sel_hi:[0,1]
	v_pk_mul_f32 v[98:99], v[22:23], v[84:85]
	v_pk_mul_f32 v[100:101], v[20:21], v[86:87]
	global_store_dwordx4 v[38:39], v[98:101], off offset:3072 sc1
	v_mul_f32_e32 v22, 0x45800000, v15
	v_cndmask_b32_e32 v22, v15, v22, vcc
	v_pk_mul_f32 v[24:25], v[22:23], v[30:31] op_sel_hi:[0,1]
	v_pk_mul_f32 v[26:27], v[22:23], v[46:47] op_sel_hi:[0,1]
	v_lshl_add_u64 v[20:21], v[88:89], 0, s[2:3]
	v_pk_mul_f32 v[102:103], v[26:27], v[72:73]
	v_pk_mul_f32 v[104:105], v[24:25], v[74:75]
	global_store_dwordx4 v[20:21], v[102:105], off sc1
	v_pk_mul_f32 v[24:25], v[22:23], v[32:33] op_sel_hi:[0,1]
	v_pk_mul_f32 v[26:27], v[22:23], v[48:49] op_sel_hi:[0,1]
	v_pk_mul_f32 v[106:107], v[26:27], v[76:77]
	v_pk_mul_f32 v[108:109], v[24:25], v[78:79]
	global_store_dwordx4 v[20:21], v[106:109], off offset:1024 sc1
	v_pk_mul_f32 v[24:25], v[22:23], v[34:35] op_sel_hi:[0,1]
	v_pk_mul_f32 v[26:27], v[22:23], v[50:51] op_sel_hi:[0,1]
	v_pk_mul_f32 v[110:111], v[26:27], v[80:81]
	v_pk_mul_f32 v[112:113], v[24:25], v[82:83]
	global_store_dwordx4 v[20:21], v[110:113], off offset:2048 sc1
	v_pk_mul_f32 v[24:25], v[22:23], v[36:37] op_sel_hi:[0,1]
	v_pk_mul_f32 v[22:23], v[22:23], v[52:53] op_sel_hi:[0,1]
	v_pk_mul_f32 v[114:115], v[22:23], v[84:85]
	v_pk_mul_f32 v[116:117], v[24:25], v[86:87]
	global_store_dwordx4 v[20:21], v[114:117], off offset:3072 sc1
	s_cbranch_scc1 .LBB0_1358
